# v34: v25 + router (P8) K loop: counted vmcnt waits so the next half-step's x2/weight loads stay in flight (the compiler's vmcnt(1)/vmcnt(0) drained the prefetch every iteration)
# speedup vs baseline: 1.0048x; 1.0048x over previous
; #define P8_LOAD(X, W, c) do { _Pragma("unroll") for (int i = 0; i < 2; ++i) { const int p = tid + 512 * i; X[i] = *(const u32x4*)(X2 + (size_t)(tok0 + (p >> 4)) * DM + (c) * 128 + (p & 15) * 8); } \
;         _Pragma("unroll") for (int i = 0; i < 2; ++i) { const int p = tid + 512 * i; W[i] = *(const f32x4*)(WRT + (size_t)(p >> 5) * DM + (c) * 128 + (p & 31) * 4); } } while (0)
; __device__ __forceinline__ void p8_router(const Frame& F, const KArgs& a) {
;     ...
;         __syncthreads();
;         P8_LOAD(xa, wa, 0); P8_WRITE(xa, wa, 0); P8_LOAD(xa, wa, 1);
;         f32x16 d = {}; float ss = 0.f;
;         for (int c = 0; c < 16; c += 2) {
;             if (c + 2 < 16) P8_LOAD(xb, wb, c + 2);
;             asm volatile("s_waitcnt lgkmcnt(0)\n\ts_barrier" ::: "memory");
;             P8_COMPUTE(0);
;             P8_WRITE(xa, wa, 1);
;             if (c + 3 < 16) P8_LOAD(xa, wa, c + 3);
;             asm volatile("s_waitcnt lgkmcnt(0)\n\ts_barrier" ::: "memory");
.LBB0_1517:
	s_waitcnt lgkmcnt(0)
	s_barrier
	ds_read_b128 v[58:61], v127
	ds_read_b128 v[54:57], v126
	ds_read_b128 v[50:53], v126 offset:32
	ds_read_b128 v[62:65], v127 offset:32
	s_cmp_gt_u32 s10, 13
	s_cbranch_scc1 .Lr8_last
	s_waitcnt vmcnt(4)
	s_branch .Lr8_go

; #define P8_LOAD(X, W, c) do { _Pragma("unroll") for (int i = 0; i < 2; ++i) { const int p = tid + 512 * i; X[i] = *(const u32x4*)(X2 + (size_t)(tok0 + (p >> 4)) * DM + (c) * 128 + (p & 15) * 8); } \
;         _Pragma("unroll") for (int i = 0; i < 2; ++i) { const int p = tid + 512 * i; W[i] = *(const f32x4*)(WRT + (size_t)(p >> 5) * DM + (c) * 128 + (p & 31) * 4); } } while (0)
; __device__ __forceinline__ void p8_router(const Frame& F, const KArgs& a) {
;     ...
;         __syncthreads();
;         P8_LOAD(xa, wa, 0); P8_WRITE(xa, wa, 0); P8_LOAD(xa, wa, 1);
;         f32x16 d = {}; float ss = 0.f;
;         for (int c = 0; c < 16; c += 2) {
;             if (c + 2 < 16) P8_LOAD(xb, wb, c + 2);
;             asm volatile("s_waitcnt lgkmcnt(0)\n\ts_barrier" ::: "memory");
;             P8_COMPUTE(0);
;             P8_WRITE(xa, wa, 1);
;             if (c + 3 < 16) P8_LOAD(xa, wa, c + 3);
;             asm volatile("s_waitcnt lgkmcnt(0)\n\ts_barrier" ::: "memory");
;             P8_COMPUTE(1);
;             if (c + 2 < 16) P8_WRITE(xb, wb, 0);
;         }
.Lr8_go:
	v_and_b32_e32 v74, 0xffff0000, v34
	v_lshlrev_b32_e32 v75, 16, v35
	s_waitcnt lgkmcnt(2)
	v_mfma_f32_32x32x2_f32 v[2:17], v58, v54, v[2:17]
	v_and_b32_e32 v76, 0xffff0000, v35
	v_lshlrev_b32_e32 v78, 16, v36
	v_and_b32_e32 v79, 0xffff0000, v36
	v_lshlrev_b32_e32 v80, 16, v37
	v_and_b32_e32 v77, 0xffff0000, v37
	v_and_b32_e32 v81, 0xffff0000, v38
	v_lshlrev_b32_e32 v113, 16, v39
	v_and_b32_e32 v115, 0xffff0000, v39
	v_lshlrev_b32_e32 v124, 16, v40
	s_cmp_gt_u32 s10, 12
	v_mfma_f32_32x32x2_f32 v[2:17], v59, v55, v[2:17]
	v_mfma_f32_32x32x2_f32 v[2:17], v60, v56, v[2:17]
	v_mfma_f32_32x32x2_f32 v[2:17], v61, v57, v[2:17]
	s_waitcnt lgkmcnt(0)
	v_mfma_f32_32x32x2_f32 v[2:17], v62, v50, v[2:17]
	v_mfma_f32_32x32x2_f32 v[2:17], v63, v51, v[2:17]
	v_mfma_f32_32x32x2_f32 v[2:17], v64, v52, v[2:17]
	v_mfma_f32_32x32x2_f32 v[2:17], v65, v53, v[2:17]
	ds_read_b128 v[66:69], v127 offset:64
	ds_read_b128 v[58:61], v126 offset:64
	ds_read_b128 v[62:65], v126 offset:96
	ds_read_b128 v[70:73], v127 offset:96
	s_waitcnt lgkmcnt(2)
	v_mfma_f32_32x32x2_f32 v[2:17], v66, v58, v[2:17]
	v_mfma_f32_32x32x2_f32 v[2:17], v67, v59, v[2:17]
	v_cndmask_b32_e64 v67, v79, v74, s[2:3]
	v_mfma_f32_32x32x2_f32 v[2:17], v68, v60, v[2:17]
	v_cndmask_b32_e64 v68, v80, v75, s[2:3]
	v_mfma_f32_32x32x2_f32 v[2:17], v69, v61, v[2:17]
	v_cndmask_b32_e64 v69, v77, v76, s[2:3]
	v_cndmask_b32_e64 v77, v76, v77, s[2:3]
	v_cndmask_b32_e64 v76, v75, v80, s[2:3]
	v_cndmask_b32_e64 v75, v74, v79, s[2:3]
	s_waitcnt lgkmcnt(0)
	v_mfma_f32_32x32x2_f32 v[2:17], v70, v62, v[2:17]
	v_lshlrev_b32_e32 v70, 16, v34
	v_cndmask_b32_e64 v66, v78, v70, s[2:3]
	v_cndmask_b32_e64 v74, v70, v78, s[2:3]
	ds_write_b128 v132, v[66:69] offset:33792
	ds_write_b128 v133, v[74:77] offset:33792
	v_and_b32_e32 v70, 0xffff0000, v40
	v_and_b32_e32 v74, 0xffff0000, v41
	v_cndmask_b32_e64 v69, v74, v115, s[2:3]
	v_cndmask_b32_e64 v67, v70, v81, s[2:3]
	v_mfma_f32_32x32x2_f32 v[2:17], v71, v63, v[2:17]
	v_lshlrev_b32_e32 v71, 16, v38
	v_cndmask_b32_e64 v66, v124, v71, s[2:3]
	v_mfma_f32_32x32x2_f32 v[2:17], v72, v64, v[2:17]
	v_lshlrev_b32_e32 v72, 16, v41
	v_cndmask_b32_e64 v68, v72, v113, s[2:3]
	ds_write_b128 v134, v[66:69] offset:33792
	v_cndmask_b32_e64 v69, v115, v74, s[2:3]
	v_cndmask_b32_e64 v68, v113, v72, s[2:3]
	v_cndmask_b32_e64 v67, v81, v70, s[2:3]
	v_cndmask_b32_e64 v66, v71, v124, s[2:3]
	ds_write_b128 v135, v[66:69] offset:33792
	ds_write_b128 v136, v[42:45] offset:16896
	ds_write_b128 v137, v[46:49] offset:16896
	v_mfma_f32_32x32x2_f32 v[2:17], v73, v65, v[2:17]
	s_cbranch_scc1 .LBB0_1519
	v_lshl_add_u64 v[34:35], s[72:73], 0, v[122:123]
	v_add_co_u32_e32 v34, vcc, 0x35c00000, v34
	v_lshl_add_u64 v[36:37], s[72:73], 0, v[120:121]
	s_nop 0
	v_addc_co_u32_e32 v35, vcc, 0, v35, vcc
	v_add_co_u32_e32 v38, vcc, 0x35c00000, v36
	v_lshl_add_u64 v[42:43], s[72:73], 0, v[116:117]
	s_nop 0
	v_addc_co_u32_e32 v39, vcc, 0, v37, vcc
	v_add_co_u32_e32 v42, vcc, 0xba100000, v42
	v_lshl_add_u64 v[44:45], s[72:73], 0, v[118:119]
	s_nop 0
	v_addc_co_u32_e32 v43, vcc, 0, v43, vcc
	v_add_co_u32_e32 v46, vcc, 0xba100000, v44
	global_load_dwordx4 v[34:37], v[34:35], off offset:768
	s_nop 0
	global_load_dwordx4 v[38:41], v[38:39], off offset:768
	v_addc_co_u32_e32 v47, vcc, 0, v45, vcc
	global_load_dwordx4 v[42:45], v[42:43], off offset:1536
	s_nop 0
	global_load_dwordx4 v[46:49], v[46:47], off offset:1536
.LBB0_1519:
	s_waitcnt lgkmcnt(0)
	s_barrier
	ds_read_b128 v[74:77], v127 offset:16896
	ds_read_b128 v[70:73], v128
	ds_read_b128 v[66:69], v128 offset:32
	ds_read_b128 v[78:81], v127 offset:16928
	s_mov_b64 s[8:9], -1
	s_andn2_b64 vcc, exec, s[0:1]
	s_waitcnt lgkmcnt(2)
	v_mfma_f32_32x32x2_f32 v[2:17], v74, v70, v[2:17]
	v_mfma_f32_32x32x2_f32 v[2:17], v75, v71, v[2:17]
	v_mfma_f32_32x32x2_f32 v[2:17], v76, v72, v[2:17]
	v_mfma_f32_32x32x2_f32 v[2:17], v77, v73, v[2:17]
	s_waitcnt lgkmcnt(0)
	v_mfma_f32_32x32x2_f32 v[2:17], v78, v66, v[2:17]
	v_mfma_f32_32x32x2_f32 v[2:17], v79, v67, v[2:17]
	v_mfma_f32_32x32x2_f32 v[2:17], v80, v68, v[2:17]
	v_mfma_f32_32x32x2_f32 v[2:17], v81, v69, v[2:17]
	ds_read_b128 v[162:165], v127 offset:16960
	ds_read_b128 v[74:77], v128 offset:64
	ds_read_b128 v[78:81], v128 offset:96
	ds_read_b128 v[166:169], v127 offset:16992
	s_waitcnt lgkmcnt(2)
	v_mfma_f32_32x32x2_f32 v[2:17], v162, v74, v[2:17]
	v_mfma_f32_32x32x2_f32 v[2:17], v163, v75, v[2:17]
	v_mfma_f32_32x32x2_f32 v[2:17], v164, v76, v[2:17]
	v_mfma_f32_32x32x2_f32 v[2:17], v165, v77, v[2:17]
	s_waitcnt lgkmcnt(0)
	v_mfma_f32_32x32x2_f32 v[2:17], v166, v78, v[2:17]
	v_mfma_f32_32x32x2_f32 v[2:17], v167, v79, v[2:17]
	v_mfma_f32_32x32x2_f32 v[2:17], v168, v80, v[2:17]
	v_mfma_f32_32x32x2_f32 v[2:17], v169, v81, v[2:17]
	s_cbranch_vccnz .LBB0_1514
	s_waitcnt vmcnt(4)
	v_lshlrev_b32_e32 v113, 16, v18
	v_and_b32_e32 v115, 0xffff0000, v18
	v_lshlrev_b32_e32 v124, 16, v19
	v_and_b32_e32 v125, 0xffff0000, v19
	v_lshlrev_b32_e32 v161, 16, v20
	v_and_b32_e32 v166, 0xffff0000, v20
	v_lshlrev_b32_e32 v167, 16, v21
	v_and_b32_e32 v168, 0xffff0000, v21
	v_cndmask_b32_e64 v165, v168, v125, s[2:3]
	v_cndmask_b32_e64 v164, v167, v124, s[2:3]
	v_cndmask_b32_e64 v163, v166, v115, s[2:3]
	v_cndmask_b32_e64 v162, v161, v113, s[2:3]
	ds_write_b128 v132, v[162:165]
	v_cndmask_b32_e64 v165, v125, v168, s[2:3]
	v_cndmask_b32_e64 v164, v124, v167, s[2:3]
	v_cndmask_b32_e64 v163, v115, v166, s[2:3]
	v_cndmask_b32_e64 v162, v113, v161, s[2:3]
	v_lshlrev_b32_e32 v113, 16, v22
	v_and_b32_e32 v115, 0xffff0000, v22
	v_lshlrev_b32_e32 v124, 16, v23
	v_and_b32_e32 v125, 0xffff0000, v23
	v_lshlrev_b32_e32 v161, 16, v24
	v_and_b32_e32 v166, 0xffff0000, v24
	v_lshlrev_b32_e32 v167, 16, v25
	v_and_b32_e32 v168, 0xffff0000, v25
	ds_write_b128 v133, v[162:165]
	v_cndmask_b32_e64 v165, v168, v125, s[2:3]
	v_cndmask_b32_e64 v164, v167, v124, s[2:3]
	v_cndmask_b32_e64 v163, v166, v115, s[2:3]
	v_cndmask_b32_e64 v162, v161, v113, s[2:3]
	ds_write_b128 v134, v[162:165]
	v_cndmask_b32_e64 v165, v125, v168, s[2:3]
	v_cndmask_b32_e64 v164, v124, v167, s[2:3]
	v_cndmask_b32_e64 v163, v115, v166, s[2:3]
	v_cndmask_b32_e64 v162, v113, v161, s[2:3]
	ds_write_b128 v135, v[162:165]
	ds_write_b128 v157, v[26:29]
	ds_write_b128 v158, v[30:33]
	v_lshl_add_u64 v[118:119], v[118:119], 0, s[42:43]
	v_lshl_add_u64 v[116:117], v[116:117], 0, s[42:43]
	v_lshl_add_u64 v[120:121], v[120:121], 0, s[44:45]
	v_lshl_add_u64 v[122:123], v[122:123], 0, s[44:45]
	s_add_i32 s10, s10, 2
	s_mov_b64 s[8:9], 0
	s_branch .LBB0_1514
